# v56 + gate/up GEMM without the epilogue alignment barriers (halves keep their one-barrier offset across units; leading half takes one extra barrier at phase end)
# baseline (speedup 1.0000x reference)
; #define PG8_BAR __builtin_amdgcn_s_barrier()
; __device__ __forceinline__ float sigm(float x) { return __builtin_amdgcn_rcpf(1.0f + __builtin_amdgcn_exp2f(-1.4426950408889634f * x)); }
; __device__ __forceinline__ u32x4 pack8(const f32x4 a, const f32x4 b) { u32x4 w; w.x = cvt_pk_bf16(a[0], a[1]); w.y = cvt_pk_bf16(a[2], a[3]); w.z = cvt_pk_bf16(b[0], b[1]); w.w = cvt_pk_bf16(b[2], b[3]); return w; }
; template <class Epi, class Sched, bool ALIGN_EPI = false, bool SP2 = false>
; __device__ __forceinline__ void gemm_phase(PG8_LAS unsigned char* lds, const Gemm g, const Sched& S, const Epi& E) {
;     ...
;         if constexpr (ALIGN_EPI) { if (wr == 0) PG8_BAR; }
;         if constexpr (!Epi::AFTER_DRAIN) { E(acc, cur, wr, wc, fr, fq); S.done(cur); }
;     __device__ __forceinline__ void operator()(const f32x4 (&acc)[2][2][4][2], const Unit& u, int wr, int wc, int fr, int fq) const {
;         const int row0 = u.pm * BM + wr * 64 + fr, col0 = u.pn * HALF + wc * 32 + 8 * fq;
; #pragma unroll
;         for (int ai = 0; ai < 2; ++ai)
; #pragma unroll
;             for (int m = 0; m < 4; ++m) {
;                 bf16_t* rowp = O + (size_t)(row0 + ai * HALF + m * 16) * ldc + col0;
;                 f32x4 h[2];
; #pragma unroll
;                 for (int n = 0; n < 2; ++n) { const f32x4 gt = acc[ai][0][m][n], up = acc[ai][1][m][n];
; #pragma unroll
;                     for (int e = 0; e < 4; ++e) h[n][e] = gt[e] * sigm(gt[e]) * up[e]; }
;                 *(u32x4*)rowp = pack8(h[0], h[1]);
;             }
.Lpeel_exit_0:
.LBB0_156:
	v_pk_mul_f32 v[160:161], v[128:129], s[82:83] op_sel:[0,1] op_sel_hi:[1,1]
	v_pk_mul_f32 v[162:163], v[130:131], s[82:83] op_sel:[0,1] op_sel_hi:[1,1]
	v_pk_mul_f32 v[164:165], v[120:121], s[82:83] op_sel:[0,1] op_sel_hi:[1,1]
	v_pk_mul_f32 v[166:167], v[122:123], s[82:83] op_sel:[0,1] op_sel_hi:[1,1]
	v_exp_f32_e32 v160, v160
	v_exp_f32_e32 v161, v161
	v_exp_f32_e32 v162, v162
	v_exp_f32_e32 v163, v163
	v_exp_f32_e32 v164, v164
	v_exp_f32_e32 v165, v165
	v_exp_f32_e32 v166, v166
	v_exp_f32_e32 v167, v167
	v_pk_add_f32 v[160:161], v[160:161], 1.0 op_sel_hi:[1,0]
	v_pk_add_f32 v[162:163], v[162:163], 1.0 op_sel_hi:[1,0]
	v_pk_add_f32 v[164:165], v[164:165], 1.0 op_sel_hi:[1,0]
	v_pk_add_f32 v[166:167], v[166:167], 1.0 op_sel_hi:[1,0]
	v_rcp_f32_e32 v160, v160
	v_rcp_f32_e32 v161, v161
	v_rcp_f32_e32 v162, v162
	v_rcp_f32_e32 v163, v163
	v_rcp_f32_e32 v164, v164
	v_rcp_f32_e32 v165, v165
	v_rcp_f32_e32 v166, v166
	v_rcp_f32_e32 v167, v167
	v_pk_mul_f32 v[160:161], v[128:129], v[160:161]
	v_pk_mul_f32 v[162:163], v[130:131], v[162:163]
	v_pk_mul_f32 v[164:165], v[120:121], v[164:165]
	v_pk_mul_f32 v[166:167], v[122:123], v[166:167]
	v_pk_mul_f32 v[124:125], v[160:161], v[124:125]
	v_pk_mul_f32 v[126:127], v[162:163], v[126:127]
	v_pk_mul_f32 v[120:121], v[164:165], v[116:117]
	v_pk_mul_f32 v[128:129], v[166:167], v[118:119]
	v_lshl_or_b32 v152, s21, 7, v148
	v_lshl_add_u32 v150, s20, 8, v2
	v_ashrrev_i32_e32 v153, 31, v152
	v_mov_b64_e32 v[144:145], s[8:9]
	v_mad_i64_i32 v[154:155], s[20:21], v150, s82, v[144:145]
	s_andn2_b64 vcc, exec, s[2:3]
	v_lshlrev_b64 v[116:117], 1, v[152:153]
	v_lshl_add_u64 v[122:123], v[154:155], 0, v[116:117]
	v_cvt_pk_bf16_f32 v118, v124, v125
	v_cvt_pk_bf16_f32 v119, v126, v127
	v_cvt_pk_bf16_f32 v120, v120, v121
	v_cvt_pk_bf16_f32 v121, v128, v129
	flat_store_dwordx4 v[122:123], v[118:121] sc1
	s_nop 1
	v_pk_mul_f32 v[160:161], v[112:113], s[82:83] op_sel:[0,1] op_sel_hi:[1,1]
	v_pk_mul_f32 v[162:163], v[114:115], s[82:83] op_sel:[0,1] op_sel_hi:[1,1]
	v_pk_mul_f32 v[164:165], v[104:105], s[82:83] op_sel:[0,1] op_sel_hi:[1,1]
	v_pk_mul_f32 v[166:167], v[106:107], s[82:83] op_sel:[0,1] op_sel_hi:[1,1]
	v_exp_f32_e32 v160, v160
	v_exp_f32_e32 v161, v161
	v_exp_f32_e32 v162, v162
	v_exp_f32_e32 v163, v163
	v_exp_f32_e32 v164, v164
	v_exp_f32_e32 v165, v165
	v_exp_f32_e32 v166, v166
	v_exp_f32_e32 v167, v167
	v_pk_add_f32 v[160:161], v[160:161], 1.0 op_sel_hi:[1,0]
	v_pk_add_f32 v[162:163], v[162:163], 1.0 op_sel_hi:[1,0]
	v_pk_add_f32 v[164:165], v[164:165], 1.0 op_sel_hi:[1,0]
	v_pk_add_f32 v[166:167], v[166:167], 1.0 op_sel_hi:[1,0]
	v_rcp_f32_e32 v160, v160
	v_rcp_f32_e32 v161, v161
	v_rcp_f32_e32 v162, v162
	v_rcp_f32_e32 v163, v163
	v_rcp_f32_e32 v164, v164
	v_rcp_f32_e32 v165, v165
	v_rcp_f32_e32 v166, v166
	v_rcp_f32_e32 v167, v167
	v_pk_mul_f32 v[160:161], v[112:113], v[160:161]
	v_pk_mul_f32 v[162:163], v[114:115], v[162:163]
	v_pk_mul_f32 v[164:165], v[104:105], v[164:165]
	v_pk_mul_f32 v[166:167], v[106:107], v[166:167]
	v_pk_mul_f32 v[108:109], v[160:161], v[108:109]
	v_pk_mul_f32 v[110:111], v[162:163], v[110:111]
	v_pk_mul_f32 v[112:113], v[164:165], v[100:101]
	v_mul_f32_e32 v106, v166, v102
	v_mul_f32_e32 v103, v167, v103
	v_or_b32_e32 v118, 16, v150
	v_mad_i64_i32 v[118:119], s[20:21], v118, s82, v[144:145]
	v_lshl_add_u64 v[104:105], v[118:119], 0, v[116:117]
	v_cvt_pk_bf16_f32 v100, v108, v109
	v_cvt_pk_bf16_f32 v101, v110, v111
	v_cvt_pk_bf16_f32 v102, v112, v113
	v_cvt_pk_bf16_f32 v103, v106, v103
	flat_store_dwordx4 v[104:105], v[100:103] sc1
	s_nop 1
	v_pk_mul_f32 v[160:161], v[96:97], s[82:83] op_sel:[0,1] op_sel_hi:[1,1]
	v_pk_mul_f32 v[162:163], v[98:99], s[82:83] op_sel:[0,1] op_sel_hi:[1,1]
	v_pk_mul_f32 v[164:165], v[88:89], s[82:83] op_sel:[0,1] op_sel_hi:[1,1]
	v_pk_mul_f32 v[166:167], v[90:91], s[82:83] op_sel:[0,1] op_sel_hi:[1,1]
	v_exp_f32_e32 v160, v160
	v_exp_f32_e32 v161, v161
	v_exp_f32_e32 v162, v162
	v_exp_f32_e32 v163, v163
	v_exp_f32_e32 v164, v164
	v_exp_f32_e32 v165, v165
	v_exp_f32_e32 v166, v166
	v_exp_f32_e32 v167, v167
	v_pk_add_f32 v[160:161], v[160:161], 1.0 op_sel_hi:[1,0]
	v_pk_add_f32 v[162:163], v[162:163], 1.0 op_sel_hi:[1,0]
	v_pk_add_f32 v[164:165], v[164:165], 1.0 op_sel_hi:[1,0]
	v_pk_add_f32 v[166:167], v[166:167], 1.0 op_sel_hi:[1,0]
	v_rcp_f32_e32 v160, v160
	v_rcp_f32_e32 v161, v161
	v_rcp_f32_e32 v162, v162
	v_rcp_f32_e32 v163, v163
	v_rcp_f32_e32 v164, v164
	v_rcp_f32_e32 v165, v165
	v_rcp_f32_e32 v166, v166
	v_rcp_f32_e32 v167, v167
	v_pk_mul_f32 v[160:161], v[96:97], v[160:161]
	v_pk_mul_f32 v[162:163], v[98:99], v[162:163]
	v_pk_mul_f32 v[164:165], v[88:89], v[164:165]
	v_pk_mul_f32 v[166:167], v[90:91], v[166:167]
	v_pk_mul_f32 v[92:93], v[160:161], v[92:93]
	v_pk_mul_f32 v[94:95], v[162:163], v[94:95]
	v_pk_mul_f32 v[96:97], v[164:165], v[84:85]
	v_mul_f32_e32 v90, v166, v86
	v_mul_f32_e32 v87, v167, v87
	v_or_b32_e32 v100, 32, v150
	v_mad_i64_i32 v[100:101], s[20:21], v100, s82, v[144:145]
	v_lshl_add_u64 v[88:89], v[100:101], 0, v[116:117]
	v_cvt_pk_bf16_f32 v84, v92, v93
	v_cvt_pk_bf16_f32 v85, v94, v95
	v_cvt_pk_bf16_f32 v86, v96, v97
	v_cvt_pk_bf16_f32 v87, v90, v87
	flat_store_dwordx4 v[88:89], v[84:87] sc1
	s_nop 1
	v_pk_mul_f32 v[160:161], v[80:81], s[82:83] op_sel:[0,1] op_sel_hi:[1,1]
	v_pk_mul_f32 v[162:163], v[82:83], s[82:83] op_sel:[0,1] op_sel_hi:[1,1]
	v_pk_mul_f32 v[164:165], v[72:73], s[82:83] op_sel:[0,1] op_sel_hi:[1,1]
	v_pk_mul_f32 v[166:167], v[74:75], s[82:83] op_sel:[0,1] op_sel_hi:[1,1]
	v_exp_f32_e32 v160, v160
	v_exp_f32_e32 v161, v161
	v_exp_f32_e32 v162, v162
	v_exp_f32_e32 v163, v163
; __device__ __forceinline__ unsigned cvt_pk_bf16(float lo, float hi) { unsigned r; asm volatile("v_cvt_pk_bf16_f32 %0, %1, %2" : "=v"(r) : "v"(lo), "v"(hi)); return r; }
; __device__ __forceinline__ float sigm(float x) { return __builtin_amdgcn_rcpf(1.0f + __builtin_amdgcn_exp2f(-1.4426950408889634f * x)); }
; __device__ __forceinline__ u32x4 pack8(const f32x4 a, const f32x4 b) { u32x4 w; w.x = cvt_pk_bf16(a[0], a[1]); w.y = cvt_pk_bf16(a[2], a[3]); w.z = cvt_pk_bf16(b[0], b[1]); w.w = cvt_pk_bf16(b[2], b[3]); return w; }
;     __device__ __forceinline__ void operator()(const f32x4 (&acc)[2][2][4][2], const Unit& u, int wr, int wc, int fr, int fq) const {
;     ...
;                 bf16_t* rowp = O + (size_t)(row0 + ai * HALF + m * 16) * ldc + col0;
;                 f32x4 h[2];
; #pragma unroll
;                 for (int n = 0; n < 2; ++n) { const f32x4 gt = acc[ai][0][m][n], up = acc[ai][1][m][n];
; #pragma unroll
;                     for (int e = 0; e < 4; ++e) h[n][e] = gt[e] * sigm(gt[e]) * up[e]; }
;                 *(u32x4*)rowp = pack8(h[0], h[1]);
	v_exp_f32_e32 v164, v164
	v_exp_f32_e32 v165, v165
	v_exp_f32_e32 v166, v166
	v_exp_f32_e32 v167, v167
	v_pk_add_f32 v[160:161], v[160:161], 1.0 op_sel_hi:[1,0]
	v_pk_add_f32 v[162:163], v[162:163], 1.0 op_sel_hi:[1,0]
	v_pk_add_f32 v[164:165], v[164:165], 1.0 op_sel_hi:[1,0]
	v_pk_add_f32 v[166:167], v[166:167], 1.0 op_sel_hi:[1,0]
	v_rcp_f32_e32 v160, v160
	v_rcp_f32_e32 v161, v161
	v_rcp_f32_e32 v162, v162
	v_rcp_f32_e32 v163, v163
	v_rcp_f32_e32 v164, v164
	v_rcp_f32_e32 v165, v165
	v_rcp_f32_e32 v166, v166
	v_rcp_f32_e32 v167, v167
	v_pk_mul_f32 v[160:161], v[80:81], v[160:161]
	v_pk_mul_f32 v[162:163], v[82:83], v[162:163]
	v_pk_mul_f32 v[164:165], v[72:73], v[164:165]
	v_pk_mul_f32 v[166:167], v[74:75], v[166:167]
	v_pk_mul_f32 v[76:77], v[160:161], v[76:77]
	v_pk_mul_f32 v[78:79], v[162:163], v[78:79]
	v_pk_mul_f32 v[80:81], v[164:165], v[68:69]
	v_mul_f32_e32 v74, v166, v70
	v_mul_f32_e32 v71, v167, v71
	v_or_b32_e32 v84, 48, v150
	v_mad_i64_i32 v[84:85], s[20:21], v84, s82, v[144:145]
	v_lshl_add_u64 v[72:73], v[84:85], 0, v[116:117]
	v_cvt_pk_bf16_f32 v68, v76, v77
	v_cvt_pk_bf16_f32 v69, v78, v79
	v_cvt_pk_bf16_f32 v70, v80, v81
	v_cvt_pk_bf16_f32 v71, v74, v71
	flat_store_dwordx4 v[72:73], v[68:71] sc1
	s_nop 1
	v_pk_mul_f32 v[160:161], v[64:65], s[82:83] op_sel:[0,1] op_sel_hi:[1,1]
	v_pk_mul_f32 v[162:163], v[66:67], s[82:83] op_sel:[0,1] op_sel_hi:[1,1]
	v_pk_mul_f32 v[164:165], v[56:57], s[82:83] op_sel:[0,1] op_sel_hi:[1,1]
	v_pk_mul_f32 v[166:167], v[58:59], s[82:83] op_sel:[0,1] op_sel_hi:[1,1]
	v_exp_f32_e32 v160, v160
	v_exp_f32_e32 v161, v161
	v_exp_f32_e32 v162, v162
	v_exp_f32_e32 v163, v163
	v_exp_f32_e32 v164, v164
	v_exp_f32_e32 v165, v165
	v_exp_f32_e32 v166, v166
	v_exp_f32_e32 v167, v167
	v_pk_add_f32 v[160:161], v[160:161], 1.0 op_sel_hi:[1,0]
	v_pk_add_f32 v[162:163], v[162:163], 1.0 op_sel_hi:[1,0]
	v_pk_add_f32 v[164:165], v[164:165], 1.0 op_sel_hi:[1,0]
	v_pk_add_f32 v[166:167], v[166:167], 1.0 op_sel_hi:[1,0]
	v_rcp_f32_e32 v160, v160
	v_rcp_f32_e32 v161, v161
	v_rcp_f32_e32 v162, v162
	v_rcp_f32_e32 v163, v163
	v_rcp_f32_e32 v164, v164
	v_rcp_f32_e32 v165, v165
	v_rcp_f32_e32 v166, v166
	v_rcp_f32_e32 v167, v167
	v_pk_mul_f32 v[160:161], v[64:65], v[160:161]
	v_pk_mul_f32 v[162:163], v[66:67], v[162:163]
	v_pk_mul_f32 v[164:165], v[56:57], v[164:165]
	v_pk_mul_f32 v[166:167], v[58:59], v[166:167]
	v_pk_mul_f32 v[60:61], v[160:161], v[60:61]
	v_pk_mul_f32 v[62:63], v[162:163], v[62:63]
	v_pk_mul_f32 v[64:65], v[164:165], v[52:53]
	v_mul_f32_e32 v58, v166, v54
	v_mul_f32_e32 v55, v167, v55
	v_add_u32_e32 v68, 0x80, v150
	v_mad_i64_i32 v[68:69], s[20:21], v68, s82, v[144:145]
	v_lshl_add_u64 v[56:57], v[68:69], 0, v[116:117]
	v_cvt_pk_bf16_f32 v52, v60, v61
	v_cvt_pk_bf16_f32 v53, v62, v63
	v_cvt_pk_bf16_f32 v54, v64, v65
	v_cvt_pk_bf16_f32 v55, v58, v55
	flat_store_dwordx4 v[56:57], v[52:55] sc1
	s_nop 1
	v_pk_mul_f32 v[160:161], v[48:49], s[82:83] op_sel:[0,1] op_sel_hi:[1,1]
	v_pk_mul_f32 v[162:163], v[50:51], s[82:83] op_sel:[0,1] op_sel_hi:[1,1]
	v_pk_mul_f32 v[164:165], v[40:41], s[82:83] op_sel:[0,1] op_sel_hi:[1,1]
	v_pk_mul_f32 v[166:167], v[42:43], s[82:83] op_sel:[0,1] op_sel_hi:[1,1]
	v_exp_f32_e32 v160, v160
	v_exp_f32_e32 v161, v161
	v_exp_f32_e32 v162, v162
	v_exp_f32_e32 v163, v163
	v_exp_f32_e32 v164, v164
	v_exp_f32_e32 v165, v165
	v_exp_f32_e32 v166, v166
	v_exp_f32_e32 v167, v167
	v_pk_add_f32 v[160:161], v[160:161], 1.0 op_sel_hi:[1,0]
	v_pk_add_f32 v[162:163], v[162:163], 1.0 op_sel_hi:[1,0]
	v_pk_add_f32 v[164:165], v[164:165], 1.0 op_sel_hi:[1,0]
	v_pk_add_f32 v[166:167], v[166:167], 1.0 op_sel_hi:[1,0]
	v_rcp_f32_e32 v160, v160
	v_rcp_f32_e32 v161, v161
	v_rcp_f32_e32 v162, v162
	v_rcp_f32_e32 v163, v163
	v_rcp_f32_e32 v164, v164
	v_rcp_f32_e32 v165, v165
	v_rcp_f32_e32 v166, v166
	v_rcp_f32_e32 v167, v167
	v_pk_mul_f32 v[160:161], v[48:49], v[160:161]
	v_pk_mul_f32 v[162:163], v[50:51], v[162:163]
	v_pk_mul_f32 v[164:165], v[40:41], v[164:165]
	v_pk_mul_f32 v[166:167], v[42:43], v[166:167]
	v_pk_mul_f32 v[44:45], v[160:161], v[44:45]
	v_pk_mul_f32 v[46:47], v[162:163], v[46:47]
	v_pk_mul_f32 v[48:49], v[164:165], v[36:37]
	v_mul_f32_e32 v42, v166, v38
	v_mul_f32_e32 v39, v167, v39
	v_add_u32_e32 v52, 0x90, v150
	v_mad_i64_i32 v[52:53], s[20:21], v52, s82, v[144:145]
	v_lshl_add_u64 v[40:41], v[52:53], 0, v[116:117]
	v_cvt_pk_bf16_f32 v36, v44, v45
	v_cvt_pk_bf16_f32 v37, v46, v47
	v_cvt_pk_bf16_f32 v38, v48, v49
	v_cvt_pk_bf16_f32 v39, v42, v39
	flat_store_dwordx4 v[40:41], v[36:39] sc1
	s_nop 1
	v_pk_mul_f32 v[160:161], v[32:33], s[82:83] op_sel:[0,1] op_sel_hi:[1,1]
	v_pk_mul_f32 v[162:163], v[34:35], s[82:83] op_sel:[0,1] op_sel_hi:[1,1]
	v_pk_mul_f32 v[164:165], v[24:25], s[82:83] op_sel:[0,1] op_sel_hi:[1,1]
	v_pk_mul_f32 v[166:167], v[26:27], s[82:83] op_sel:[0,1] op_sel_hi:[1,1]
	v_exp_f32_e32 v160, v160
	v_exp_f32_e32 v161, v161
	v_exp_f32_e32 v162, v162
	v_exp_f32_e32 v163, v163
	v_exp_f32_e32 v164, v164
; #define PG8_WAIT_V(n) asm volatile("s_waitcnt vmcnt(" #n ")" ::: "memory")
; #define PG8_BAR __builtin_amdgcn_s_barrier()
; __device__ __forceinline__ float sigm(float x) { return __builtin_amdgcn_rcpf(1.0f + __builtin_amdgcn_exp2f(-1.4426950408889634f * x)); }
; __device__ __forceinline__ u32x4 pack8(const f32x4 a, const f32x4 b) { u32x4 w; w.x = cvt_pk_bf16(a[0], a[1]); w.y = cvt_pk_bf16(a[2], a[3]); w.z = cvt_pk_bf16(b[0], b[1]); w.w = cvt_pk_bf16(b[2], b[3]); return w; }
; template <class Epi, class Sched, bool ALIGN_EPI = false, bool SP2 = false>
; __device__ __forceinline__ void gemm_phase(PG8_LAS unsigned char* lds, const Gemm g, const Sched& S, const Epi& E) {
;     ...
;         cur = nxt; cA = nA; cB = nB; ++ui;
;         if constexpr (ALIGN_EPI) { if (wr == 1) PG8_BAR; }
;     }
;     PG8_WAIT_V(0);
;     if constexpr (!ALIGN_EPI) { if (wr == 0) PG8_BAR; }
;     PG8_BAR;
;     __device__ __forceinline__ void operator()(const f32x4 (&acc)[2][2][4][2], const Unit& u, int wr, int wc, int fr, int fq) const {
;     ...
;                 bf16_t* rowp = O + (size_t)(row0 + ai * HALF + m * 16) * ldc + col0;
;                 f32x4 h[2];
; #pragma unroll
;                 for (int n = 0; n < 2; ++n) { const f32x4 gt = acc[ai][0][m][n], up = acc[ai][1][m][n];
; #pragma unroll
;                     for (int e = 0; e < 4; ++e) h[n][e] = gt[e] * sigm(gt[e]) * up[e]; }
;                 *(u32x4*)rowp = pack8(h[0], h[1]);
;             }
;     }
	v_exp_f32_e32 v165, v165
	v_exp_f32_e32 v166, v166
	v_exp_f32_e32 v167, v167
	v_pk_add_f32 v[160:161], v[160:161], 1.0 op_sel_hi:[1,0]
	v_pk_add_f32 v[162:163], v[162:163], 1.0 op_sel_hi:[1,0]
	v_pk_add_f32 v[164:165], v[164:165], 1.0 op_sel_hi:[1,0]
	v_pk_add_f32 v[166:167], v[166:167], 1.0 op_sel_hi:[1,0]
	v_rcp_f32_e32 v160, v160
	v_rcp_f32_e32 v161, v161
	v_rcp_f32_e32 v162, v162
	v_rcp_f32_e32 v163, v163
	v_rcp_f32_e32 v164, v164
	v_rcp_f32_e32 v165, v165
	v_rcp_f32_e32 v166, v166
	v_rcp_f32_e32 v167, v167
	v_pk_mul_f32 v[160:161], v[32:33], v[160:161]
	v_pk_mul_f32 v[162:163], v[34:35], v[162:163]
	v_pk_mul_f32 v[164:165], v[24:25], v[164:165]
	v_pk_mul_f32 v[166:167], v[26:27], v[166:167]
	v_pk_mul_f32 v[28:29], v[160:161], v[28:29]
	v_pk_mul_f32 v[30:31], v[162:163], v[30:31]
	v_pk_mul_f32 v[32:33], v[164:165], v[20:21]
	v_mul_f32_e32 v26, v166, v22
	v_mul_f32_e32 v23, v167, v23
	v_add_u32_e32 v36, 0xa0, v150
	v_mad_i64_i32 v[36:37], s[20:21], v36, s82, v[144:145]
	v_lshl_add_u64 v[24:25], v[36:37], 0, v[116:117]
	v_cvt_pk_bf16_f32 v20, v28, v29
	v_cvt_pk_bf16_f32 v21, v30, v31
	v_cvt_pk_bf16_f32 v22, v32, v33
	v_cvt_pk_bf16_f32 v23, v26, v23
	flat_store_dwordx4 v[24:25], v[20:23] sc1
	s_nop 1
	v_pk_mul_f32 v[160:161], v[16:17], s[82:83] op_sel:[0,1] op_sel_hi:[1,1]
	v_pk_mul_f32 v[162:163], v[18:19], s[82:83] op_sel:[0,1] op_sel_hi:[1,1]
	v_pk_mul_f32 v[164:165], v[8:9], s[82:83] op_sel:[0,1] op_sel_hi:[1,1]
	v_pk_mul_f32 v[166:167], v[10:11], s[82:83] op_sel:[0,1] op_sel_hi:[1,1]
	v_exp_f32_e32 v160, v160
	v_exp_f32_e32 v161, v161
	v_exp_f32_e32 v162, v162
	v_exp_f32_e32 v163, v163
	v_exp_f32_e32 v164, v164
	v_exp_f32_e32 v165, v165
	v_exp_f32_e32 v166, v166
	v_exp_f32_e32 v167, v167
	v_pk_add_f32 v[160:161], v[160:161], 1.0 op_sel_hi:[1,0]
	v_pk_add_f32 v[162:163], v[162:163], 1.0 op_sel_hi:[1,0]
	v_pk_add_f32 v[164:165], v[164:165], 1.0 op_sel_hi:[1,0]
	v_pk_add_f32 v[166:167], v[166:167], 1.0 op_sel_hi:[1,0]
	v_rcp_f32_e32 v160, v160
	v_rcp_f32_e32 v161, v161
	v_rcp_f32_e32 v162, v162
	v_rcp_f32_e32 v163, v163
	v_rcp_f32_e32 v164, v164
	v_rcp_f32_e32 v165, v165
	v_rcp_f32_e32 v166, v166
	v_rcp_f32_e32 v167, v167
	v_pk_mul_f32 v[160:161], v[16:17], v[160:161]
	v_pk_mul_f32 v[162:163], v[18:19], v[162:163]
	v_pk_mul_f32 v[164:165], v[8:9], v[164:165]
	v_pk_mul_f32 v[166:167], v[10:11], v[166:167]
	v_pk_mul_f32 v[12:13], v[160:161], v[12:13]
	v_pk_mul_f32 v[14:15], v[162:163], v[14:15]
	v_pk_mul_f32 v[16:17], v[164:165], v[4:5]
	v_mul_f32_e32 v10, v166, v6
	v_mul_f32_e32 v7, v167, v7
	v_add_u32_e32 v20, 0xb0, v150
	v_mad_i64_i32 v[20:21], s[20:21], v20, s82, v[144:145]
	s_mov_b64 s[20:21], -1
	v_lshl_add_u64 v[8:9], v[20:21], 0, v[116:117]
	v_cvt_pk_bf16_f32 v4, v12, v13
	v_cvt_pk_bf16_f32 v5, v14, v15
	v_cvt_pk_bf16_f32 v6, v16, v17
	v_cvt_pk_bf16_f32 v7, v10, v7
	flat_store_dwordx4 v[8:9], v[4:7] sc1
	s_cbranch_vccnz .LBB0_149
	s_andn2_b64 vcc, exec, s[6:7]
	s_cbranch_vccnz .LBB0_148
	s_branch .LBB0_148
.LBB0_159:
	s_waitcnt vmcnt(0)
	s_cmp_lg_u64 s[10:11], 0
	s_cbranch_scc0 .Lgu_noalign_end
	s_barrier
.Lgu_noalign_end:
	s_barrier
.LBB0_160:
	s_cmpk_lg_i32 s1, 0x100
	s_cselect_b64 s[2:3], -1, 0
	s_cmpk_lt_i32 s30, 0x80
	s_cselect_b64 s[6:7], -1, 0
	s_or_b64 s[2:3], s[2:3], s[6:7]
	s_and_b64 vcc, exec, s[2:3]
	s_cbranch_vccnz .LBB0_599
	v_readlane_b32 s2, v253, 55
	s_cmp_eq_u32 s2, 7
	v_readlane_b32 s3, v253, 56
	s_cbranch_scc1 .LBB0_599
	s_ashr_i32 s15, s0, 6
	s_lshl_b32 s14, s30, 3
	s_add_i32 s18, s15, 0xfffffc00
	s_lshl_b32 s0, s15, 14
	s_add_i32 s17, s18, s14
	s_add_i32 s16, s0, 0
	s_cmp_lg_u32 s37, 0
	v_and_b32_e32 v37, 63, v146
	s_cbranch_scc1 .LBB0_537
	v_readlane_b32 s0, v253, 55
	v_readlane_b32 s1, v253, 56
	s_and_b32 s1, s0, 2
	v_readlane_b32 s0, v252, 0
	s_lshl_b32 s0, s0, 10
	s_cmp_lg_u32 s1, 0
	s_mov_b64 s[2:3], -1
	s_cbranch_scc0 .LBB0_289
	s_cmpk_gt_i32 s17, 0x67f
	s_cbranch_scc1 .LBB0_226
	v_readlane_b32 s3, v252, 0
	s_mul_i32 s2, s3, 0x680
	s_add_i32 s1, s2, 0x9580
	s_add_u32 s19, s4, 0x6000000
	s_addc_u32 s20, s5, 0
	s_add_u32 s21, s4, 0x8c00000
	s_addc_u32 s22, s5, 0
	s_add_u32 s23, s4, 0x9700000
	s_addc_u32 s24, s5, 0
	s_add_u32 s25, s4, 0x9b00000
	s_addc_u32 s26, s5, 0
	s_add_u32 s27, s4, 0xa800000
	s_addc_u32 s31, s5, 0
	s_add_u32 s33, s4, 0xac00000
	s_addc_u32 s34, s5, 0
	s_add_u32 s35, s4, 0x108000
	s_addc_u32 s39, s5, 0
	s_add_i32 s2, s15, s2
	s_add_i32 s2, s2, s14
	s_add_i32 s40, s2, 0xffffe700
	s_add_i32 s2, s2, 0x8f00
	s_mulk_i32 s3, 0xd00
	v_and_b32_e32 v2, 7, v146
	v_lshrrev_b32_e32 v39, 3, v37
	s_lshl_b32 s41, s2, 3
	s_lshl_b32 s42, s2, 5
	s_lshl_b32 s2, s30, 4
	v_lshlrev_b32_e32 v36, 2, v2
	v_lshl_add_u32 v44, v2, 4, s16
	v_lshlrev_b32_e32 v38, 3, v2
	v_mul_u32_u24_e32 v2, 0x420, v2
	v_lshlrev_b32_e32 v4, 2, v39
	s_add_i32 s2, s3, s2
	v_mul_u32_u24_e32 v45, 0x84, v39
	v_or_b32_e32 v46, 8, v39
	v_or_b32_e32 v47, 16, v39
	v_or_b32_e32 v48, 24, v39
	v_add3_u32 v49, s16, v2, v4
	s_lshl_b32 s43, s15, 1
	s_add_i32 s44, s2, 0x11e00
	s_branch .LBB0_167
